# recheck: single candidate extraction loop over both mask words
# speedup vs baseline: 1.0072x; 1.0072x over previous
.Lrc_skip_tile3:
.Lcx_loop:
	v_or_b32_e32 v188, v186, v187
	v_cmp_ne_u32_e32 vcc, 0, v188
	s_cbranch_vccz .Lcx_done
	s_and_saveexec_b64 s[0:1], vcc
	v_cmp_ne_u32_e32 vcc, 0, v186
	v_mov_b32_e32 v192, 64
	s_nop 0
	v_cndmask_b32_e32 v188, v187, v186, vcc
	v_cndmask_b32_e32 v192, v192, v169, vcc
	v_ffbl_b32_e32 v189, v188
	v_lshlrev_b32_e64 v190, v189, 1
	v_cndmask_b32_e32 v191, 0, v190, vcc
	v_xor_b32_e32 v186, v186, v191
	v_xor_b32_e32 v191, v190, v191
	v_xor_b32_e32 v187, v187, v191
	v_lshrrev_b32_e32 v190, 2, v189
	v_and_b32_e32 v189, 3, v189
	v_lshl_or_b32 v190, v190, 3, v189
	v_or3_b32 v189, v190, v179, v192
	s_mov_b64 s[16:17], exec
	v_mbcnt_lo_u32_b32 v190, s16, 0
	v_mbcnt_hi_u32_b32 v190, s17, v190
	v_cmp_eq_u32_e32 vcc, 0, v190
	s_and_saveexec_b64 s[14:15], vcc
	s_bcnt1_i32_b64 s16, s[16:17]
	v_mov_b32_e32 v191, s16
	ds_add_rtn_u32 v191, v248, v191
	s_or_b64 exec, exec, s[14:15]
	s_waitcnt lgkmcnt(0)
	v_readfirstlane_b32 s14, v191
	s_nop 1
	v_add_u32_e32 v190, s14, v190
	v_cmp_gt_u32_e32 vcc, s20, v190
	s_and_b64 exec, exec, vcc
	v_lshl_add_u32 v190, v190, 2, v246
	ds_write_b32 v190, v189
	s_or_b64 exec, exec, s[0:1]
	s_branch .Lcx_loop
